# baseline (speedup 1.0000x reference)
.LBB0_2:
	s_cmp_eq_u32 s36, 7
	s_cbranch_scc0 .Lprod_end
	s_cmp_lt_u32 s2, 256
	s_cbranch_scc0 .Lprod_end
	s_mov_b64 exec, -1
	buffer_wbl2 sc1
